# speedup vs baseline: 1.0125x; 1.0125x over previous
.LBB0_20:
	s_andn2_b64 vcc, exec, s[4:5]
	s_cbranch_vccnz .LBB0_27
	s_load_dwordx2 s[4:5], s[0:1], 0x0
	s_load_dwordx2 s[6:7], s[0:1], 0x18
	s_load_dwordx2 s[12:13], s[0:1], 0x10
	s_load_dwordx2 s[14:15], s[0:1], 0x28
	s_sub_u32 s2, s2, 10
	v_lshl_or_b32 v2, s2, 9, v0
	v_lshl_add_u32 v4, v0, 8, s2
	v_ashrrev_i32_e32 v5, 31, v4
	v_ashrrev_i32_e32 v3, 31, v2
	s_waitcnt lgkmcnt(0)
	v_lshl_add_u64 v[4:5], v[4:5], 2, s[4:5]
	global_load_dword v4, v[4:5], off
	v_and_b32_e32 v1, 63, v0
	v_lshl_add_u64 v[2:3], v[2:3], 2, s[6:7]
	v_cmp_eq_u32_e64 s[4:5], 0, v1
	s_waitcnt vmcnt(0)
	v_cmp_ne_u32_e32 vcc, 1, v4
	global_store_dword v[2:3], v4, off
	s_and_saveexec_b64 s[6:7], s[4:5]
	s_bcnt1_i32_b64 s3, vcc
	v_lshrrev_b32_e32 v1, 4, v0
	v_mov_b32_e32 v2, s3
	ds_write_b32 v1, v2
	s_or_b64 exec, exec, s[6:7]
	v_mov_b32_e32 v1, 0
	s_waitcnt lgkmcnt(0)
	s_barrier
	ds_read_b128 v[6:9], v1
	ds_read_b128 v[10:13], v1 offset:16
	v_cmp_eq_u32_e32 vcc, 0, v0
	s_waitcnt lgkmcnt(1)
	v_add_u32_e32 v2, v7, v6
	v_add_u32_e32 v2, v8, v2
	v_add_u32_e32 v2, v9, v2
	s_waitcnt lgkmcnt(0)
	v_add_u32_e32 v2, v10, v2
	v_add_u32_e32 v2, v11, v2
	v_add_u32_e32 v2, v12, v2
	v_add_u32_e32 v2, v13, v2
	s_and_saveexec_b64 s[4:5], vcc
	s_cbranch_execz .LBB0_25
	s_ashr_i32 s3, s2, 31
	s_lshl_b64 s[2:3], s[2:3], 2
	s_add_u32 s2, s12, s2
	s_addc_u32 s3, s13, s3
	global_store_dword v1, v2, s[2:3]
.LBB0_25:
	s_or_b64 exec, exec, s[4:5]
	v_min_i32_e32 v1, 0x1ff, v2
	v_cmp_le_i32_e32 vcc, v0, v1
	s_and_saveexec_b64 s[2:3], vcc
	s_cbranch_execz .LBB0_27
	v_ashrrev_i32_e32 v5, 31, v4
	v_mov_b32_e32 v2, 1
	v_lshl_add_u64 v[0:1], s[14:15], 0, v[4:5]
	global_store_byte v[0:1], v2, off

	.amdhsa_kernel _Z6k_prepPKiPKfPiS3_P15HIP_vector_typeIjLj4EEPh
		.amdhsa_group_segment_fixed_size 32
		.amdhsa_private_segment_fixed_size 0
		.amdhsa_kernarg_size 48
		.amdhsa_user_sgpr_count 2
		.amdhsa_user_sgpr_dispatch_ptr 0
		.amdhsa_user_sgpr_queue_ptr 0
		.amdhsa_user_sgpr_kernarg_segment_ptr 1
		.amdhsa_user_sgpr_dispatch_id 0
		.amdhsa_user_sgpr_kernarg_preload_length 0
		.amdhsa_user_sgpr_kernarg_preload_offset 0
		.amdhsa_user_sgpr_private_segment_size 0
		.amdhsa_uses_dynamic_stack 0
		.amdhsa_enable_private_segment 0
		.amdhsa_system_sgpr_workgroup_id_x 1
		.amdhsa_system_sgpr_workgroup_id_y 0
		.amdhsa_system_sgpr_workgroup_id_z 0
		.amdhsa_system_sgpr_workgroup_info 0
		.amdhsa_system_vgpr_workitem_id 0
		.amdhsa_next_free_vgpr 36
		.amdhsa_next_free_sgpr 16
		.amdhsa_accum_offset 36
		.amdhsa_reserve_vcc 1
		.amdhsa_float_round_mode_32 0
		.amdhsa_float_round_mode_16_64 0
		.amdhsa_float_denorm_mode_32 3
		.amdhsa_float_denorm_mode_16_64 3
		.amdhsa_dx10_clamp 1
		.amdhsa_ieee_mode 1
		.amdhsa_fp16_overflow 0
		.amdhsa_tg_split 0
		.amdhsa_exception_fp_ieee_invalid_op 0
		.amdhsa_exception_fp_denorm_src 0
		.amdhsa_exception_fp_ieee_div_zero 0
		.amdhsa_exception_fp_ieee_overflow 0
		.amdhsa_exception_fp_ieee_underflow 0
		.amdhsa_exception_fp_ieee_inexact 0
		.amdhsa_exception_int_div_zero 0
	.end_amdhsa_kernel

amdhsa.kernels:
  - .agpr_count:     0
    .args:
      - .actual_access:  read_only
        .address_space:  global
        .offset:         0
        .size:           8
        .value_kind:     global_buffer
      - .actual_access:  read_only
        .address_space:  global
        .offset:         8
        .size:           8
        .value_kind:     global_buffer
      - .actual_access:  write_only
        .address_space:  global
        .offset:         16
        .size:           8
        .value_kind:     global_buffer
      - .actual_access:  write_only
        .address_space:  global
        .offset:         24
        .size:           8
        .value_kind:     global_buffer
      - .actual_access:  write_only
        .address_space:  global
        .offset:         32
        .size:           8
        .value_kind:     global_buffer
      - .actual_access:  write_only
        .address_space:  global
        .offset:         40
        .size:           8
        .value_kind:     global_buffer
    .group_segment_fixed_size: 32
    .kernarg_segment_align: 8
    .kernarg_segment_size: 48
    .language:       OpenCL C
    .language_version:
      - 2
      - 0
    .max_flat_workgroup_size: 512
    .name:           _Z6k_prepPKiPKfPiS3_P15HIP_vector_typeIjLj4EEPh
    .private_segment_fixed_size: 0
    .sgpr_count:     22
    .sgpr_spill_count: 0
    .symbol:         _Z6k_prepPKiPKfPiS3_P15HIP_vector_typeIjLj4EEPh.kd
    .uniform_work_group_size: 1
    .uses_dynamic_stack: false
    .vgpr_count:     36
    .vgpr_spill_count: 0
    .wavefront_size: 64
  - .agpr_count:     0
    .args:
      - .actual_access:  read_only
        .address_space:  global
        .offset:         0
        .size:           8
        .value_kind:     global_buffer
      - .actual_access:  read_only
        .address_space:  global
        .offset:         8
        .size:           8
        .value_kind:     global_buffer
      - .actual_access:  read_only
        .address_space:  global
        .offset:         16
        .size:           8
        .value_kind:     global_buffer
      - .actual_access:  write_only
        .address_space:  global
        .offset:         24
        .size:           8
        .value_kind:     global_buffer
      - .actual_access:  read_only
        .address_space:  global
        .offset:         32
        .size:           8
        .value_kind:     global_buffer
    .group_segment_fixed_size: 16384
    .kernarg_segment_align: 8
    .kernarg_segment_size: 40
    .language:       OpenCL C
    .language_version:
      - 2
      - 0
    .max_flat_workgroup_size: 256
    .name:           _Z6k_gemmPKfS0_PK15HIP_vector_typeIjLj4EEPDF16_PKh
    .private_segment_fixed_size: 0
    .sgpr_count:     54
    .sgpr_spill_count: 0
    .symbol:         _Z6k_gemmPKfS0_PK15HIP_vector_typeIjLj4EEPDF16_PKh.kd
    .uniform_work_group_size: 1
    .uses_dynamic_stack: false
    .vgpr_count:     256
    .vgpr_spill_count: 0
    .wavefront_size: 64
  - .agpr_count:     0
    .args:
      - .actual_access:  read_only
        .address_space:  global
        .offset:         0
        .size:           8
        .value_kind:     global_buffer
      - .actual_access:  read_only
        .address_space:  global
        .offset:         8
        .size:           8
        .value_kind:     global_buffer
      - .actual_access:  read_only
        .address_space:  global
        .offset:         16
        .size:           8
        .value_kind:     global_buffer
      - .actual_access:  read_only
        .address_space:  global
        .offset:         24
        .size:           8
        .value_kind:     global_buffer
      - .actual_access:  read_only
        .address_space:  global
        .offset:         32
        .size:           8
        .value_kind:     global_buffer
      - .actual_access:  read_only
        .address_space:  global
        .offset:         40
        .size:           8
        .value_kind:     global_buffer
      - .actual_access:  write_only
        .address_space:  global
        .offset:         48
        .size:           8
        .value_kind:     global_buffer
    .group_segment_fixed_size: 4096
    .kernarg_segment_align: 8
    .kernarg_segment_size: 56
    .language:       OpenCL C
    .language_version:
      - 2
      - 0
    .max_flat_workgroup_size: 1024
    .name:           _Z6k_poolPKDF16_PKiS2_PKfS4_S4_Pf
    .private_segment_fixed_size: 0
    .sgpr_count:     30
    .sgpr_spill_count: 0
    .symbol:         _Z6k_poolPKDF16_PKiS2_PKfS4_S4_Pf.kd
    .uniform_work_group_size: 1
    .uses_dynamic_stack: false
    .vgpr_count:     64
    .vgpr_spill_count: 0
    .wavefront_size: 64
